# v8 + DPP/permlane wave reductions in LN1/LN2 row loops (replacing ds_bpermute butterflies)
# speedup vs baseline: 1.0050x; 1.0050x over previous
.LBB0_1232:
	v_lshlrev_b32_e32 v72, 16, v76
	v_and_b32_e32 v73, 0xffff0000, v76
	v_lshlrev_b32_e32 v96, 16, v74
	v_and_b32_e32 v97, 0xffff0000, v74
	v_lshlrev_b32_e32 v76, 16, v77
	v_and_b32_e32 v77, 0xffff0000, v77
	v_lshlrev_b32_e32 v74, 16, v75
	v_and_b32_e32 v75, 0xffff0000, v75
	v_pk_fma_f32 v[72:73], v[72:73], s[36:37], v[96:97] op_sel_hi:[1,0,1]
	v_pk_fma_f32 v[76:77], v[76:77], s[36:37], v[74:75] op_sel_hi:[1,0,1]
	v_lshlrev_b32_e32 v74, 16, v80
	v_and_b32_e32 v75, 0xffff0000, v80
	v_lshlrev_b32_e32 v96, 16, v78
	v_and_b32_e32 v97, 0xffff0000, v78
	v_lshlrev_b32_e32 v80, 16, v81
	v_and_b32_e32 v81, 0xffff0000, v81
	v_lshlrev_b32_e32 v78, 16, v79
	v_and_b32_e32 v79, 0xffff0000, v79
	v_pk_fma_f32 v[74:75], v[74:75], s[36:37], v[96:97] op_sel_hi:[1,0,1]
	v_pk_fma_f32 v[80:81], v[80:81], s[36:37], v[78:79] op_sel_hi:[1,0,1]
	v_lshlrev_b32_e32 v78, 16, v84
	v_and_b32_e32 v79, 0xffff0000, v84
	v_lshlrev_b32_e32 v96, 16, v82
	v_and_b32_e32 v97, 0xffff0000, v82
	v_lshlrev_b32_e32 v84, 16, v85
	v_and_b32_e32 v85, 0xffff0000, v85
	v_lshlrev_b32_e32 v82, 16, v83
	v_and_b32_e32 v83, 0xffff0000, v83
	v_pk_fma_f32 v[78:79], v[78:79], s[36:37], v[96:97] op_sel_hi:[1,0,1]
	v_pk_fma_f32 v[84:85], v[84:85], s[36:37], v[82:83] op_sel_hi:[1,0,1]
	v_lshlrev_b32_e32 v82, 16, v88
	v_and_b32_e32 v83, 0xffff0000, v88
	v_lshlrev_b32_e32 v96, 16, v86
	v_and_b32_e32 v97, 0xffff0000, v86
	v_lshlrev_b32_e32 v88, 16, v89
	v_and_b32_e32 v89, 0xffff0000, v89
	v_lshlrev_b32_e32 v86, 16, v87
	v_and_b32_e32 v87, 0xffff0000, v87
	v_pk_fma_f32 v[82:83], v[82:83], s[36:37], v[96:97] op_sel_hi:[1,0,1]
	v_pk_fma_f32 v[88:89], v[88:89], s[36:37], v[86:87] op_sel_hi:[1,0,1]
	v_lshlrev_b32_e32 v86, 16, v92
	v_and_b32_e32 v87, 0xffff0000, v92
	v_lshlrev_b32_e32 v96, 16, v90
	v_and_b32_e32 v97, 0xffff0000, v90
	v_lshlrev_b32_e32 v92, 16, v93
	v_and_b32_e32 v93, 0xffff0000, v93
	v_lshlrev_b32_e32 v90, 16, v91
	v_and_b32_e32 v91, 0xffff0000, v91
	v_pk_fma_f32 v[86:87], v[86:87], s[36:37], v[96:97] op_sel_hi:[1,0,1]
	v_pk_fma_f32 v[92:93], v[92:93], s[36:37], v[90:91] op_sel_hi:[1,0,1]
	v_lshlrev_b32_e32 v90, 16, v94
	v_and_b32_e32 v91, 0xffff0000, v94
	v_lshlrev_b32_e32 v96, 16, v12
	v_and_b32_e32 v97, 0xffff0000, v12
	v_lshlrev_b32_e32 v94, 16, v95
	v_and_b32_e32 v95, 0xffff0000, v95
	v_lshlrev_b32_e32 v12, 16, v13
	v_and_b32_e32 v13, 0xffff0000, v13
	v_pk_fma_f32 v[90:91], v[90:91], s[36:37], v[96:97] op_sel_hi:[1,0,1]
	v_pk_fma_f32 v[96:97], v[94:95], s[36:37], v[12:13] op_sel_hi:[1,0,1]
	v_lshlrev_b32_e32 v12, 16, v98
	v_and_b32_e32 v13, 0xffff0000, v98
	v_lshlrev_b32_e32 v94, 16, v8
	v_and_b32_e32 v95, 0xffff0000, v8
	v_pk_fma_f32 v[94:95], v[12:13], s[36:37], v[94:95] op_sel_hi:[1,0,1]
	v_lshlrev_b32_e32 v12, 16, v99
	v_and_b32_e32 v13, 0xffff0000, v99
	v_lshlrev_b32_e32 v8, 16, v9
	v_and_b32_e32 v9, 0xffff0000, v9
	v_pk_fma_f32 v[100:101], v[12:13], s[36:37], v[8:9] op_sel_hi:[1,0,1]
	v_lshlrev_b32_e32 v8, 16, v10
	v_and_b32_e32 v9, 0xffff0000, v10
	v_lshlrev_b32_e32 v12, 16, v6
	v_and_b32_e32 v13, 0xffff0000, v6
	v_pk_fma_f32 v[98:99], v[8:9], s[36:37], v[12:13] op_sel_hi:[1,0,1]
	v_lshlrev_b32_e32 v8, 16, v11
	v_and_b32_e32 v9, 0xffff0000, v11
	v_lshlrev_b32_e32 v6, 16, v7
	v_and_b32_e32 v7, 0xffff0000, v7
	v_pk_fma_f32 v[102:103], v[8:9], s[36:37], v[6:7] op_sel_hi:[1,0,1]
	v_mov_b32_e32 v8, v74
	v_mov_b32_e32 v9, v80
	v_mov_b32_e32 v10, v75
	v_mov_b32_e32 v11, v81
	v_pk_add_f32 v[8:9], v[8:9], v[10:11]
	v_pk_add_f32 v[10:11], v[78:79], v[78:79] op_sel:[0,1] op_sel_hi:[1,0]
	v_pk_add_f32 v[12:13], v[84:85], v[84:85] op_sel:[0,1] op_sel_hi:[1,0]
	v_add_f32_e32 v6, v76, v77
	v_add_f32_e32 v7, v72, v73
	v_pk_add_f32 v[10:11], v[10:11], v[12:13]
	v_mov_b32_e32 v12, v82
	v_mov_b32_e32 v13, v88
	v_mov_b32_e32 v122, v83
	v_mov_b32_e32 v123, v89
	v_add_f32_e32 v6, v7, v6
	v_pk_add_f32 v[12:13], v[12:13], v[122:123]
	v_pk_add_f32 v[122:123], v[86:87], v[86:87] op_sel_hi:[0,1]
	v_pk_add_f32 v[124:125], v[92:93], v[92:93] op_sel_hi:[0,1]
	v_add_f32_e32 v7, 0, v6
	v_add_f32_e32 v6, v8, v9
	v_mov_b32_e32 v122, v94
	v_mov_b32_e32 v124, v95
	v_add_f32_e32 v9, 0, v6
	v_pk_add_f32 v[122:123], v[122:123], v[124:125]
	v_mov_b32_e32 v124, v100
	v_mov_b32_e32 v125, v10
	v_mov_b32_e32 v6, v101
	v_pk_add_f32 v[12:13], v[12:13], v[12:13] op_sel_hi:[0,1]
	v_pk_add_f32 v[126:127], v[90:91], v[90:91] op_sel_hi:[0,1]
	v_pk_add_f32 v[128:129], v[96:97], v[96:97] op_sel_hi:[0,1]
	v_pk_add_f32 v[6:7], v[124:125], v[6:7]
	v_mov_b32_e32 v126, v98
	v_pk_add_f32 v[6:7], v[122:123], v[6:7]
	v_mov_b32_e32 v128, v99
	v_mov_b32_e32 v12, v102
	v_mov_b32_e32 v8, v103
	v_add_f32_e32 v10, v6, v7
	v_pk_add_f32 v[6:7], v[126:127], v[128:129]
	v_pk_add_f32 v[8:9], v[12:13], v[8:9]
	global_load_dwordx4 v[122:125], v[40:41], off
	global_load_dwordx4 v[126:129], v[40:41], off offset:1024
	global_load_dwordx4 v[130:133], v[42:43], off
	global_load_dwordx4 v[134:137], v[42:43], off offset:1024
	v_pk_add_f32 v[6:7], v[6:7], v[8:9]
	s_ashr_i32 s61, s60, 31
	v_add_f32_e32 v6, v6, v7
	s_nop 1
	v_mov_b32_dpp v7, v10 quad_perm:[1,0,3,2] row_mask:0xf bank_mask:0xf
	s_nop 1
	v_mov_b32_dpp v8, v6 quad_perm:[1,0,3,2] row_mask:0xf bank_mask:0xf
	s_add_i32 s14, s2, 2
	s_lshl_b64 s[24:25], s[60:61], 11
	s_add_u32 s24, s12, s24
	s_waitcnt lgkmcnt(1)
	v_add_f32_e32 v7, v10, v7
	s_waitcnt lgkmcnt(0)
	v_add_f32_e32 v6, v6, v8
	s_nop 1
	v_mov_b32_dpp v8, v7 quad_perm:[2,3,0,1] row_mask:0xf bank_mask:0xf
	s_nop 1
	v_mov_b32_dpp v9, v6 quad_perm:[2,3,0,1] row_mask:0xf bank_mask:0xf
	s_addc_u32 s25, s13, s25
	v_cmp_eq_u32_e32 vcc, s2, v63
	s_waitcnt lgkmcnt(1)
	v_add_f32_e32 v7, v7, v8
	s_waitcnt lgkmcnt(0)
	v_add_f32_e32 v6, v6, v9
	s_nop 1
	v_mov_b32_dpp v8, v7 row_half_mirror row_mask:0xf bank_mask:0xf
	s_nop 1
	v_mov_b32_dpp v9, v6 row_half_mirror row_mask:0xf bank_mask:0xf
	s_waitcnt lgkmcnt(1)
	v_add_f32_e32 v7, v7, v8
	s_waitcnt lgkmcnt(0)
	v_add_f32_e32 v6, v6, v9
	s_nop 1
	v_mov_b32_dpp v8, v7 row_mirror row_mask:0xf bank_mask:0xf
	s_nop 1
	v_mov_b32_dpp v9, v6 row_mirror row_mask:0xf bank_mask:0xf
	s_waitcnt lgkmcnt(1)
	v_add_f32_e32 v7, v7, v8
	s_waitcnt lgkmcnt(0)
	v_add_f32_e32 v6, v6, v9
	v_mov_b32_e32 v8, v7
	s_nop 1
	v_permlane16_swap_b32_e32 v8, v7
	v_mov_b32_e32 v9, v6
	s_nop 1
	v_permlane16_swap_b32_e32 v9, v6
	s_waitcnt lgkmcnt(1)
	v_add_f32_e32 v59, v7, v8
	s_waitcnt lgkmcnt(0)
	v_add_f32_e32 v60, v6, v9
	global_load_dwordx4 v[138:141], v[40:41], off offset:2048
	global_load_dwordx4 v[6:9], v[40:41], off offset:3072
	global_load_dwordx4 v[142:145], v[42:43], off offset:2048
	global_load_dwordx4 v[10:13], v[42:43], off offset:3072
	v_mov_b32_e32 v146, v59
	s_nop 1
	v_permlane32_swap_b32_e32 v146, v59
	v_mov_b32_e32 v147, v60
	s_nop 1
	v_permlane32_swap_b32_e32 v147, v60
	s_waitcnt lgkmcnt(1)
	v_add_f32_e32 v59, v59, v146
	v_fmac_f32_e32 v77, 0xba800000, v59
	v_fmac_f32_e32 v73, 0xba800000, v59
	s_waitcnt lgkmcnt(0)
	v_add_f32_e32 v60, v60, v147
	v_fmamk_f32 v76, v59, 0xba800000, v76
	v_fmamk_f32 v72, v59, 0xba800000, v72
	v_mul_f32_e32 v146, v73, v73
	v_mul_f32_e32 v147, v77, v77
	v_fmac_f32_e32 v81, 0xba800000, v60
	v_fmac_f32_e32 v75, 0xba800000, v60
	v_fmac_f32_e32 v146, v72, v72
	v_fmac_f32_e32 v147, v76, v76
	v_fmamk_f32 v80, v60, 0xba800000, v80
	v_fmamk_f32 v74, v60, 0xba800000, v74
	v_add_f32_e32 v146, v146, v147
	v_mul_f32_e32 v147, v75, v75
	v_mul_f32_e32 v148, v81, v81
	v_fmac_f32_e32 v147, v74, v74
	v_fmac_f32_e32 v148, v80, v80
	v_fmac_f32_e32 v85, 0xba800000, v59
	v_fmac_f32_e32 v79, 0xba800000, v59
	v_add_f32_e32 v147, v147, v148
	v_fmamk_f32 v84, v59, 0xba800000, v84
	v_fmamk_f32 v78, v59, 0xba800000, v78
	v_mul_f32_e32 v148, v79, v79
	v_mul_f32_e32 v149, v85, v85
	v_fmac_f32_e32 v148, v78, v78
	v_fmac_f32_e32 v149, v84, v84
	v_fmac_f32_e32 v89, 0xba800000, v60
	v_fmac_f32_e32 v83, 0xba800000, v60
	v_add_f32_e32 v148, v148, v149
	v_fmamk_f32 v88, v60, 0xba800000, v88
	v_fmamk_f32 v82, v60, 0xba800000, v82
	v_add_f32_e32 v146, v146, v148
	v_mul_f32_e32 v148, v83, v83
	v_mul_f32_e32 v149, v89, v89
	v_fmac_f32_e32 v148, v82, v82
	v_fmac_f32_e32 v149, v88, v88
	v_fmac_f32_e32 v93, 0xba800000, v59
	v_fmac_f32_e32 v87, 0xba800000, v59
	v_add_f32_e32 v149, v148, v149
	v_fmamk_f32 v92, v59, 0xba800000, v92
	v_fmamk_f32 v86, v59, 0xba800000, v86
	v_mul_f32_e32 v148, v87, v87
	v_mul_f32_e32 v150, v93, v93
	v_fmac_f32_e32 v148, v86, v86
	v_fmac_f32_e32 v150, v92, v92
	v_add_f32_e32 v148, v148, v150
	v_fmac_f32_e32 v101, 0xba800000, v59
	v_fmac_f32_e32 v95, 0xba800000, v59
	v_add_f32_e32 v146, v148, v146
	v_fmamk_f32 v100, v59, 0xba800000, v100
	v_fmamk_f32 v94, v59, 0xba800000, v94
	v_mul_f32_e32 v148, v95, v95
	v_mul_f32_e32 v150, v101, v101
	v_fmac_f32_e32 v97, 0xba800000, v60
	v_fmac_f32_e32 v91, 0xba800000, v60
	v_fmac_f32_e32 v148, v94, v94
	v_fmac_f32_e32 v150, v100, v100
	v_fmamk_f32 v96, v60, 0xba800000, v96
	v_fmamk_f32 v90, v60, 0xba800000, v90
	v_mul_f32_e32 v151, v91, v91
	v_mul_f32_e32 v153, v97, v97
	v_fmamk_f32 v103, v60, 0xba800000, v103
	v_fmac_f32_e32 v102, 0xba800000, v60
	v_fmamk_f32 v99, v60, 0xba800000, v99
	v_fmac_f32_e32 v98, 0xba800000, v60
	v_add_f32_e32 v148, v148, v150
	v_fmac_f32_e32 v151, v90, v90
	v_fmac_f32_e32 v153, v96, v96
	v_add_f32_e32 v154, v148, v146
	v_mul_f32_e32 v150, v98, v98
	v_mul_f32_e32 v152, v99, v99
	v_mul_f32_e32 v146, v102, v102
	v_mul_f32_e32 v148, v103, v103
	v_pk_add_f32 v[150:151], v[150:151], v[152:153]
	v_pk_add_f32 v[146:147], v[146:147], v[148:149]
	s_nop 1
	v_mov_b32_dpp v148, v154 quad_perm:[1,0,3,2] row_mask:0xf bank_mask:0xf
	v_pk_add_f32 v[146:147], v[150:151], v[146:147]
	v_mul_f32_e32 v150, 0x3a800000, v60
	v_add_f32_e32 v146, v146, v147
	s_nop 1
	v_mov_b32_dpp v147, v146 quad_perm:[1,0,3,2] row_mask:0xf bank_mask:0xf
	s_waitcnt lgkmcnt(1)
	v_add_f32_e32 v148, v154, v148
	s_nop 1
	v_mov_b32_dpp v149, v148 quad_perm:[2,3,0,1] row_mask:0xf bank_mask:0xf
	v_mul_f32_e32 v59, 0x3a800000, v59
	s_waitcnt lgkmcnt(1)
	v_add_f32_e32 v146, v146, v147
	s_nop 1
	v_mov_b32_dpp v147, v146 quad_perm:[2,3,0,1] row_mask:0xf bank_mask:0xf
	s_waitcnt lgkmcnt(1)
	v_add_f32_e32 v148, v148, v149
	s_nop 1
	v_mov_b32_dpp v149, v148 row_half_mirror row_mask:0xf bank_mask:0xf
	s_waitcnt lgkmcnt(1)
	v_add_f32_e32 v146, v146, v147
	s_nop 1
	v_mov_b32_dpp v147, v146 row_half_mirror row_mask:0xf bank_mask:0xf
	s_waitcnt lgkmcnt(1)
	v_add_f32_e32 v148, v148, v149
	s_nop 1
	v_mov_b32_dpp v149, v148 row_mirror row_mask:0xf bank_mask:0xf
	s_waitcnt lgkmcnt(1)
	v_add_f32_e32 v146, v146, v147
	s_nop 1
	v_mov_b32_dpp v147, v146 row_mirror row_mask:0xf bank_mask:0xf
	s_waitcnt lgkmcnt(1)
	v_add_f32_e32 v148, v148, v149
	v_mov_b32_e32 v149, v148
	s_nop 1
	v_permlane16_swap_b32_e32 v149, v148
	s_waitcnt lgkmcnt(1)
	v_add_f32_e32 v146, v146, v147
	v_mov_b32_e32 v147, v146
	s_nop 1
	v_permlane16_swap_b32_e32 v147, v146
	s_waitcnt lgkmcnt(1)
	v_add_f32_e32 v148, v148, v149
	v_mov_b32_e32 v149, v148
	s_nop 1
	v_permlane32_swap_b32_e32 v149, v148
	s_waitcnt lgkmcnt(1)
	v_add_f32_e32 v146, v146, v147
	v_mov_b32_e32 v147, v146
	s_nop 1
	v_permlane32_swap_b32_e32 v147, v146
	s_waitcnt lgkmcnt(1)
	v_add_f32_e32 v60, v148, v149
	v_fmamk_f32 v60, v60, 0x3a800000, v226
	v_rsq_f32_e32 v60, v60
	s_waitcnt lgkmcnt(0)
	v_add_f32_e32 v146, v146, v147
	v_fmamk_f32 v146, v146, 0x3a800000, v226
	v_rsq_f32_e32 v146, v146
	v_pk_mul_f32 v[100:101], v[100:101], v[60:61] op_sel_hi:[1,0]
	v_pk_mul_f32 v[72:73], v[72:73], v[60:61] op_sel_hi:[1,0]
	s_waitcnt vmcnt(0)
	v_pk_fma_f32 v[100:101], v[8:9], v[100:101], v[12:13]
	v_pk_mul_f32 v[102:103], v[102:103], v[146:147] op_sel_hi:[1,0]
	v_pk_mul_f32 v[76:77], v[76:77], v[60:61] op_sel_hi:[1,0]
	v_pk_fma_f32 v[8:9], v[8:9], v[102:103], v[12:13]
	v_lshl_add_u64 v[12:13], s[24:25], 0, v[50:51]
	s_add_i32 s24, s60, 1
	v_pk_mul_f32 v[94:95], v[94:95], v[60:61] op_sel_hi:[1,0]
	v_pk_mul_f32 v[98:99], v[98:99], v[146:147] op_sel_hi:[1,0]
	s_ashr_i32 s25, s24, 31
	v_pk_fma_f32 v[76:77], v[124:125], v[76:77], v[132:133]
	v_pk_fma_f32 v[72:73], v[122:123], v[72:73], v[130:131]
	v_pk_mul_f32 v[78:79], v[78:79], v[60:61] op_sel_hi:[1,0]
	v_pk_mul_f32 v[84:85], v[84:85], v[60:61] op_sel_hi:[1,0]
	v_pk_fma_f32 v[94:95], v[6:7], v[94:95], v[10:11]
	v_pk_fma_f32 v[6:7], v[6:7], v[98:99], v[10:11]
	v_cvt_pk_bf16_f32 v10, v72, v73
	v_cvt_pk_bf16_f32 v11, v76, v77
	s_lshl_b64 s[24:25], s[24:25], 11
	v_pk_fma_f32 v[84:85], v[128:129], v[84:85], v[136:137]
	v_pk_fma_f32 v[78:79], v[126:127], v[78:79], v[134:135]
	v_pk_mul_f32 v[86:87], v[86:87], v[60:61] op_sel_hi:[1,0]
	v_pk_mul_f32 v[92:93], v[92:93], v[60:61] op_sel_hi:[1,0]
	global_store_dwordx2 v[12:13], v[10:11], off
	v_cvt_pk_bf16_f32 v10, v78, v79
	v_cvt_pk_bf16_f32 v11, v84, v85
	s_add_u32 s24, s12, s24
	v_pk_fma_f32 v[92:93], v[140:141], v[92:93], v[144:145]
	v_pk_fma_f32 v[86:87], v[138:139], v[86:87], v[142:143]
	global_store_dwordx2 v[12:13], v[10:11], off offset:512
	v_cvt_pk_bf16_f32 v10, v86, v87
	v_cvt_pk_bf16_f32 v11, v92, v93
	s_addc_u32 s25, s13, s25
	v_pk_mul_f32 v[74:75], v[74:75], v[146:147] op_sel_hi:[1,0]
	v_pk_mul_f32 v[80:81], v[80:81], v[146:147] op_sel_hi:[1,0]
	global_store_dwordx2 v[12:13], v[10:11], off offset:1024
	v_cvt_pk_bf16_f32 v10, v94, v95
	v_cvt_pk_bf16_f32 v11, v100, v101
	global_store_dwordx2 v[12:13], v[10:11], off offset:1536
	v_lshl_add_u64 v[12:13], s[24:25], 0, v[50:51]
	v_cvt_pk_bf16_f32 v6, v6, v7
	v_cvt_pk_bf16_f32 v7, v8, v9
	v_pk_fma_f32 v[80:81], v[124:125], v[80:81], v[132:133]
	v_pk_fma_f32 v[74:75], v[122:123], v[74:75], v[130:131]
	v_pk_mul_f32 v[82:83], v[82:83], v[146:147] op_sel_hi:[1,0]
	v_pk_mul_f32 v[88:89], v[88:89], v[146:147] op_sel_hi:[1,0]
	v_cvt_pk_bf16_f32 v10, v74, v75
	v_cvt_pk_bf16_f32 v11, v80, v81
	global_store_dwordx2 v[12:13], v[6:7], off offset:1536
	v_cndmask_b32_e32 v6, v62, v60, vcc
	v_cndmask_b32_e32 v7, v61, v59, vcc
	v_cmp_eq_u32_e32 vcc, s2, v121
	v_pk_fma_f32 v[88:89], v[128:129], v[88:89], v[136:137]
	v_pk_fma_f32 v[82:83], v[126:127], v[82:83], v[134:135]
	v_pk_mul_f32 v[90:91], v[90:91], v[146:147] op_sel_hi:[1,0]
	v_pk_mul_f32 v[96:97], v[96:97], v[146:147] op_sel_hi:[1,0]
	global_store_dwordx2 v[12:13], v[10:11], off
	v_cvt_pk_bf16_f32 v10, v82, v83
	v_cvt_pk_bf16_f32 v11, v88, v89
	v_cndmask_b32_e32 v62, v6, v146, vcc
	v_cndmask_b32_e32 v61, v7, v150, vcc
	s_and_b64 vcc, exec, s[46:47]
	v_pk_fma_f32 v[96:97], v[140:141], v[96:97], v[144:145]
	v_pk_fma_f32 v[90:91], v[138:139], v[90:91], v[142:143]
	global_store_dwordx2 v[12:13], v[10:11], off offset:512
	v_cvt_pk_bf16_f32 v10, v90, v91
	v_cvt_pk_bf16_f32 v11, v96, v97
	global_store_dwordx2 v[12:13], v[10:11], off offset:1024
	s_cbranch_vccnz .LBB0_1234
	v_mov_b64_e32 v[78:79], v[34:35]
	v_mov_b64_e32 v[86:87], v[64:65]
	v_mov_b64_e32 v[12:13], v[68:69]
	v_mov_b64_e32 v[6:7], v[70:71]
	v_mov_b64_e32 v[74:75], v[18:19]
	v_mov_b64_e32 v[82:83], v[22:23]
	v_mov_b64_e32 v[90:91], v[24:25]
	v_mov_b64_e32 v[8:9], v[26:27]
	v_mov_b64_e32 v[80:81], v[28:29]
	v_mov_b64_e32 v[88:89], v[30:31]
	v_mov_b64_e32 v[94:95], v[36:37]
	v_mov_b64_e32 v[10:11], v[66:67]
	v_mov_b64_e32 v[76:77], v[14:15]
	v_mov_b64_e32 v[84:85], v[16:17]
	v_mov_b64_e32 v[92:93], v[20:21]
	v_mov_b64_e32 v[98:99], v[32:33]
	s_mov_b32 s2, s14
	s_branch .LBB0_1230

.LBB0_1572:
	s_waitcnt vmcnt(31)
	v_cvt_pk_f32_fp8_e32 v[98:99], v81
	v_lshlrev_b32_e32 v82, 16, v72
	v_and_b32_e32 v83, 0xffff0000, v72
	v_pk_mul_f32 v[82:83], v[82:83], s[36:37] op_sel_hi:[1,0]
	v_lshlrev_b32_e32 v72, 16, v73
	v_pk_fma_f32 v[82:83], v[98:99], v[30:31], v[82:83] op_sel_hi:[1,0,1]
	v_cvt_pk_f32_fp8_sdwa v[98:99], v81 src0_sel:WORD_1
	v_and_b32_e32 v73, 0xffff0000, v73
	v_pk_mul_f32 v[72:73], v[72:73], s[36:37] op_sel_hi:[1,0]
	v_lshlrev_b32_e32 v84, 16, v70
	v_pk_fma_f32 v[72:73], v[98:99], v[30:31], v[72:73] op_sel_hi:[1,0,1]
	s_waitcnt vmcnt(30)
	v_cvt_pk_f32_fp8_e32 v[98:99], v80
	v_cvt_pk_f32_fp8_sdwa v[80:81], v80 src0_sel:WORD_1
	v_and_b32_e32 v85, 0xffff0000, v70
	v_lshlrev_b32_e32 v70, 16, v71
	v_and_b32_e32 v71, 0xffff0000, v71
	v_pk_mul_f32 v[70:71], v[70:71], s[36:37] op_sel_hi:[1,0]
	v_lshlrev_b32_e32 v86, 16, v68
	v_pk_fma_f32 v[70:71], v[80:81], v[26:27], v[70:71] op_sel_hi:[1,0,1]
	s_waitcnt vmcnt(29)
	v_cvt_pk_f32_fp8_e32 v[80:81], v79
	v_and_b32_e32 v87, 0xffff0000, v68
	v_pk_mul_f32 v[86:87], v[86:87], s[36:37] op_sel_hi:[1,0]
	v_lshlrev_b32_e32 v68, 16, v69
	v_pk_fma_f32 v[80:81], v[80:81], v[30:31], v[86:87] op_sel_hi:[1,0,1]
	v_cvt_pk_f32_fp8_sdwa v[86:87], v79 src0_sel:WORD_1
	v_and_b32_e32 v69, 0xffff0000, v69
	v_pk_mul_f32 v[68:69], v[68:69], s[36:37] op_sel_hi:[1,0]
	v_lshlrev_b32_e32 v88, 16, v66
	v_pk_fma_f32 v[68:69], v[86:87], v[30:31], v[68:69] op_sel_hi:[1,0,1]
	s_waitcnt vmcnt(28)
	v_cvt_pk_f32_fp8_e32 v[86:87], v78
	v_and_b32_e32 v89, 0xffff0000, v66
	v_pk_mul_f32 v[88:89], v[88:89], s[36:37] op_sel_hi:[1,0]
	v_lshlrev_b32_e32 v90, 16, v64
	v_pk_fma_f32 v[86:87], v[86:87], v[26:27], v[88:89] op_sel_hi:[1,0,1]
	s_waitcnt vmcnt(27)
	v_cvt_pk_f32_fp8_sdwa v[88:89], v77 src0_sel:WORD_1
	v_and_b32_e32 v91, 0xffff0000, v64
	v_lshlrev_b32_e32 v64, 16, v65
	v_and_b32_e32 v65, 0xffff0000, v65
	v_pk_mul_f32 v[64:65], v[64:65], s[36:37] op_sel_hi:[1,0]
	v_cvt_pk_f32_fp8_sdwa v[78:79], v78 src0_sel:WORD_1
	v_pk_fma_f32 v[64:65], v[88:89], v[30:31], v[64:65] op_sel_hi:[1,0,1]
	s_waitcnt vmcnt(26)
	v_cvt_pk_f32_fp8_e32 v[88:89], v76
	v_lshlrev_b32_e32 v66, 16, v67
	v_and_b32_e32 v67, 0xffff0000, v67
	v_lshlrev_b32_e32 v92, 16, v62
	v_and_b32_e32 v93, 0xffff0000, v62
	v_pk_mul_f32 v[66:67], v[66:67], s[36:37] op_sel_hi:[1,0]
	v_pk_mul_f32 v[92:93], v[92:93], s[36:37] op_sel_hi:[1,0]
	v_pk_fma_f32 v[66:67], v[78:79], v[26:27], v[66:67] op_sel_hi:[1,0,1]
	v_cvt_pk_f32_fp8_e32 v[78:79], v77
	v_pk_fma_f32 v[88:89], v[88:89], v[26:27], v[92:93] op_sel_hi:[1,0,1]
	v_cvt_pk_f32_fp8_sdwa v[76:77], v76 src0_sel:WORD_1
	s_waitcnt vmcnt(25)
	v_cvt_pk_f32_fp8_sdwa v[92:93], v57 src0_sel:WORD_1
	v_lshlrev_b32_e32 v62, 16, v63
	v_and_b32_e32 v63, 0xffff0000, v63
	v_lshlrev_b32_e32 v96, 16, v58
	v_and_b32_e32 v97, 0xffff0000, v58
	v_lshlrev_b32_e32 v58, 16, v59
	v_and_b32_e32 v59, 0xffff0000, v59
	v_pk_mul_f32 v[90:91], v[90:91], s[36:37] op_sel_hi:[1,0]
	v_pk_mul_f32 v[62:63], v[62:63], s[36:37] op_sel_hi:[1,0]
	v_pk_mul_f32 v[58:59], v[58:59], s[36:37] op_sel_hi:[1,0]
	v_pk_fma_f32 v[78:79], v[78:79], v[30:31], v[90:91] op_sel_hi:[1,0,1]
	v_pk_fma_f32 v[62:63], v[76:77], v[26:27], v[62:63] op_sel_hi:[1,0,1]
	s_waitcnt vmcnt(24)
	v_cvt_pk_f32_fp8_e32 v[76:77], v75
	v_cvt_pk_f32_fp8_sdwa v[90:91], v75 src0_sel:WORD_1
	v_pk_fma_f32 v[58:59], v[92:93], v[26:27], v[58:59] op_sel_hi:[1,0,1]
	s_waitcnt vmcnt(23)
	v_cvt_pk_f32_fp8_e32 v[92:93], v74
	v_cvt_pk_f32_fp8_sdwa v[74:75], v74 src0_sel:WORD_1
	v_lshlrev_b32_e32 v94, 16, v60
	v_and_b32_e32 v95, 0xffff0000, v60
	v_lshlrev_b32_e32 v60, 16, v61
	v_and_b32_e32 v61, 0xffff0000, v61
	v_pk_mul_f32 v[60:61], v[60:61], s[36:37] op_sel_hi:[1,0]
	v_pk_fma_f32 v[72:73], v[74:75], v[30:31], v[72:73] op_sel:[0,1,0]
	v_pk_fma_f32 v[60:61], v[90:91], v[30:31], v[60:61] op_sel_hi:[1,0,1]
	v_cvt_pk_f32_fp8_e32 v[90:91], v57
	s_waitcnt vmcnt(22)
	v_cvt_pk_f32_fp8_e32 v[74:75], v56
	v_cvt_pk_f32_fp8_sdwa v[56:57], v56 src0_sel:WORD_1
	v_pk_mul_f32 v[94:95], v[94:95], s[36:37] op_sel_hi:[1,0]
	v_pk_fma_f32 v[82:83], v[92:93], v[30:31], v[82:83] op_sel:[0,1,0]
	v_pk_fma_f32 v[76:77], v[76:77], v[30:31], v[94:95] op_sel_hi:[1,0,1]
	v_pk_fma_f32 v[56:57], v[56:57], v[26:27], v[70:71] op_sel:[0,1,0]
	s_waitcnt vmcnt(21)
	v_cvt_pk_f32_fp8_e32 v[70:71], v55
	v_pk_mul_f32 v[84:85], v[84:85], s[36:37] op_sel_hi:[1,0]
	v_pk_mul_f32 v[96:97], v[96:97], s[36:37] op_sel_hi:[1,0]
	v_pk_fma_f32 v[84:85], v[98:99], v[26:27], v[84:85] op_sel_hi:[1,0,1]
	v_pk_fma_f32 v[70:71], v[70:71], v[30:31], v[80:81] op_sel:[0,1,0]
	v_cvt_pk_f32_fp8_sdwa v[80:81], v55 src0_sel:WORD_1
	v_pk_fma_f32 v[90:91], v[90:91], v[26:27], v[96:97] op_sel_hi:[1,0,1]
	v_pk_fma_f32 v[74:75], v[74:75], v[26:27], v[84:85] op_sel:[0,1,0]
	s_andn2_b64 vcc, exec, s[46:47]
	v_pk_fma_f32 v[68:69], v[80:81], v[30:31], v[68:69] op_sel:[0,1,0]
	s_waitcnt vmcnt(20)
	v_cvt_pk_f32_fp8_e32 v[80:81], v54
	v_cvt_pk_f32_fp8_sdwa v[54:55], v54 src0_sel:WORD_1
	v_pk_fma_f32 v[80:81], v[80:81], v[26:27], v[86:87] op_sel:[0,1,0]
	v_pk_fma_f32 v[54:55], v[54:55], v[26:27], v[66:67] op_sel:[0,1,0]
	s_waitcnt vmcnt(19)
	v_cvt_pk_f32_fp8_e32 v[66:67], v53
	v_pk_fma_f32 v[66:67], v[66:67], v[30:31], v[78:79] op_sel:[0,1,0]
	v_cvt_pk_f32_fp8_sdwa v[78:79], v53 src0_sel:WORD_1
	v_pk_fma_f32 v[64:65], v[78:79], v[30:31], v[64:65] op_sel:[0,1,0]
	s_waitcnt vmcnt(18)
	v_cvt_pk_f32_fp8_e32 v[78:79], v52
	v_cvt_pk_f32_fp8_sdwa v[52:53], v52 src0_sel:WORD_1
	v_pk_fma_f32 v[78:79], v[78:79], v[26:27], v[88:89] op_sel:[0,1,0]
	v_pk_fma_f32 v[52:53], v[52:53], v[26:27], v[62:63] op_sel:[0,1,0]
	s_waitcnt vmcnt(16)
	v_cvt_pk_f32_fp8_e32 v[62:63], v51
	v_pk_fma_f32 v[62:63], v[62:63], v[30:31], v[76:77] op_sel:[0,1,0]
	v_cvt_pk_f32_fp8_sdwa v[76:77], v51 src0_sel:WORD_1
	v_pk_fma_f32 v[30:31], v[76:77], v[30:31], v[60:61] op_sel:[0,1,0]
	v_cvt_pk_f32_fp8_e32 v[60:61], v49
	v_cvt_pk_f32_fp8_sdwa v[76:77], v49 src0_sel:WORD_1
	v_pk_fma_f32 v[60:61], v[60:61], v[26:27], v[90:91] op_sel:[0,1,0]
	v_pk_fma_f32 v[26:27], v[76:77], v[26:27], v[58:59] op_sel:[0,1,0]
	s_waitcnt vmcnt(15)
	v_cvt_pk_f32_fp8_e32 v[58:59], v50
	v_cvt_pk_f32_fp8_sdwa v[50:51], v50 src0_sel:WORD_1
	v_pk_fma_f32 v[58:59], v[58:59], v[32:33], v[82:83] op_sel_hi:[1,0,1]
	v_pk_fma_f32 v[50:51], v[50:51], v[32:33], v[72:73] op_sel_hi:[1,0,1]
	s_waitcnt vmcnt(14)
	v_cvt_pk_f32_fp8_e32 v[72:73], v48
	v_cvt_pk_f32_fp8_sdwa v[48:49], v48 src0_sel:WORD_1
	v_pk_fma_f32 v[72:73], v[72:73], v[28:29], v[74:75] op_sel_hi:[1,0,1]
	v_pk_fma_f32 v[48:49], v[48:49], v[28:29], v[56:57] op_sel_hi:[1,0,1]
	s_waitcnt vmcnt(13)
	v_cvt_pk_f32_fp8_e32 v[56:57], v47
	v_pk_fma_f32 v[56:57], v[56:57], v[32:33], v[70:71] op_sel_hi:[1,0,1]
	v_cvt_pk_f32_fp8_sdwa v[70:71], v47 src0_sel:WORD_1
	v_pk_fma_f32 v[68:69], v[70:71], v[32:33], v[68:69] op_sel_hi:[1,0,1]
	s_waitcnt vmcnt(12)
	v_cvt_pk_f32_fp8_e32 v[70:71], v46
	v_cvt_pk_f32_fp8_sdwa v[46:47], v46 src0_sel:WORD_1
	v_pk_fma_f32 v[74:75], v[70:71], v[28:29], v[80:81] op_sel_hi:[1,0,1]
	v_pk_fma_f32 v[46:47], v[46:47], v[28:29], v[54:55] op_sel_hi:[1,0,1]
	s_waitcnt vmcnt(11)
	v_cvt_pk_f32_fp8_e32 v[54:55], v45
	v_pk_fma_f32 v[54:55], v[54:55], v[32:33], v[66:67] op_sel_hi:[1,0,1]
	v_cvt_pk_f32_fp8_sdwa v[66:67], v45 src0_sel:WORD_1
	v_pk_fma_f32 v[76:77], v[66:67], v[32:33], v[64:65] op_sel_hi:[1,0,1]
	s_waitcnt vmcnt(10)
	v_cvt_pk_f32_fp8_e32 v[64:65], v44
	v_cvt_pk_f32_fp8_sdwa v[44:45], v44 src0_sel:WORD_1
	v_pk_fma_f32 v[80:81], v[64:65], v[28:29], v[78:79] op_sel_hi:[1,0,1]
	v_pk_fma_f32 v[44:45], v[44:45], v[28:29], v[52:53] op_sel_hi:[1,0,1]
	s_waitcnt vmcnt(8)
	v_cvt_pk_f32_fp8_e32 v[52:53], v43
	v_pk_fma_f32 v[52:53], v[52:53], v[32:33], v[62:63] op_sel_hi:[1,0,1]
	v_cvt_pk_f32_fp8_sdwa v[62:63], v43 src0_sel:WORD_1
	v_pk_fma_f32 v[30:31], v[62:63], v[32:33], v[30:31] op_sel_hi:[1,0,1]
	v_cvt_pk_f32_fp8_e32 v[62:63], v42
	v_cvt_pk_f32_fp8_sdwa v[42:43], v42 src0_sel:WORD_1
	v_mov_b32_e32 v32, v29
	v_pk_fma_f32 v[88:89], v[62:63], v[28:29], v[60:61] op_sel_hi:[1,0,1]
	v_pk_fma_f32 v[26:27], v[42:43], v[28:29], v[26:27] op_sel_hi:[1,0,1]
	s_waitcnt vmcnt(7)
	v_cvt_pk_f32_fp8_e32 v[42:43], v41
	v_mov_b32_e32 v28, v33
	v_pk_fma_f32 v[60:61], v[42:43], v[28:29], v[58:59] op_sel_hi:[1,0,1]
	v_cvt_pk_f32_fp8_sdwa v[42:43], v41 src0_sel:WORD_1
	v_mov_b32_e32 v92, v60
	v_pk_fma_f32 v[62:63], v[42:43], v[28:29], v[50:51] op_sel_hi:[1,0,1]
	s_waitcnt vmcnt(6)
	v_cvt_pk_f32_fp8_e32 v[42:43], v40
	v_cvt_pk_f32_fp8_sdwa v[40:41], v40 src0_sel:WORD_1
	v_pk_mov_b32 v[90:91], v[60:61], v[62:63] op_sel:[1,0]
	v_mov_b32_e32 v93, v63
	v_pk_fma_f32 v[58:59], v[42:43], v[32:33], v[72:73] op_sel_hi:[1,0,1]
	v_pk_fma_f32 v[70:71], v[40:41], v[32:33], v[48:49] op_sel_hi:[1,0,1]
	s_waitcnt vmcnt(5)
	v_cvt_pk_f32_fp8_e32 v[40:41], v39
	v_pk_add_f32 v[90:91], v[90:91], v[92:93]
	v_pk_mov_b32 v[92:93], v[58:59], v[70:71] op_sel:[1,0]
	v_mov_b32_e32 v94, v58
	v_pk_fma_f32 v[66:67], v[40:41], v[28:29], v[56:57] op_sel_hi:[1,0,1]
	v_cvt_pk_f32_fp8_sdwa v[40:41], v39 src0_sel:WORD_1
	v_mov_b32_e32 v95, v71
	v_pk_add_f32 v[92:93], v[92:93], v[94:95]
	v_mov_b32_e32 v96, v66
	v_pk_fma_f32 v[68:69], v[40:41], v[28:29], v[68:69] op_sel_hi:[1,0,1]
	s_waitcnt vmcnt(4)
	v_cvt_pk_f32_fp8_e32 v[40:41], v38
	v_cvt_pk_f32_fp8_sdwa v[38:39], v38 src0_sel:WORD_1
	v_pk_mov_b32 v[94:95], v[66:67], v[68:69] op_sel:[1,0]
	v_mov_b32_e32 v97, v69
	v_pk_fma_f32 v[64:65], v[40:41], v[32:33], v[74:75] op_sel_hi:[1,0,1]
	v_pk_fma_f32 v[78:79], v[38:39], v[32:33], v[46:47] op_sel_hi:[1,0,1]
	s_waitcnt vmcnt(3)
	v_cvt_pk_f32_fp8_e32 v[38:39], v37
	v_add_f32_e32 v90, v90, v91
	v_pk_add_f32 v[94:95], v[94:95], v[96:97]
	v_add_f32_e32 v91, 0, v90
	v_pk_fma_f32 v[74:75], v[38:39], v[28:29], v[54:55] op_sel_hi:[1,0,1]
	v_cvt_pk_f32_fp8_sdwa v[38:39], v37 src0_sel:WORD_1
	v_add_f32_e32 v90, v92, v93
	v_pk_add_f32 v[94:95], v[94:95], v[94:95] op_sel_hi:[0,1]
	v_pk_mov_b32 v[96:97], v[64:65], v[78:79] op_sel:[1,0]
	v_pk_fma_f32 v[76:77], v[38:39], v[28:29], v[76:77] op_sel_hi:[1,0,1]
	s_waitcnt vmcnt(2)
	v_cvt_pk_f32_fp8_e32 v[38:39], v36
	v_cvt_pk_f32_fp8_sdwa v[36:37], v36 src0_sel:WORD_1
	v_mov_b32_e32 v98, v64
	v_mov_b32_e32 v99, v79
	v_pk_fma_f32 v[72:73], v[38:39], v[32:33], v[80:81] op_sel_hi:[1,0,1]
	v_pk_fma_f32 v[86:87], v[36:37], v[32:33], v[44:45] op_sel_hi:[1,0,1]
	s_waitcnt vmcnt(0)
	v_cvt_pk_f32_fp8_e32 v[36:37], v35
	v_add_f32_e32 v93, 0, v90
	v_pk_add_f32 v[96:97], v[96:97], v[98:99]
	v_add_f32_e32 v99, v74, v75
	v_pk_fma_f32 v[82:83], v[36:37], v[28:29], v[52:53] op_sel_hi:[1,0,1]
	v_cvt_pk_f32_fp8_sdwa v[36:37], v35 src0_sel:WORD_1
	v_add_f32_e32 v101, v76, v77
	v_mov_b32_e32 v94, v82
	v_mov_b32_e32 v90, v83
	v_pk_fma_f32 v[84:85], v[36:37], v[28:29], v[30:31] op_sel_hi:[1,0,1]
	v_cvt_pk_f32_fp8_e32 v[28:29], v34
	v_mov_b32_e32 v98, v84
	v_mov_b32_e32 v100, v85
	v_pk_add_f32 v[96:97], v[96:97], v[96:97] op_sel_hi:[0,1]
	v_pk_fma_f32 v[80:81], v[28:29], v[32:33], v[88:89] op_sel_hi:[1,0,1]
	v_cvt_pk_f32_fp8_sdwa v[28:29], v34 src0_sel:WORD_1
	v_pk_add_f32 v[90:91], v[94:95], v[90:91]
	v_pk_add_f32 v[94:95], v[98:99], v[100:101]
	v_add_f32_e32 v103, v72, v73
	v_pk_fma_f32 v[88:89], v[28:29], v[32:33], v[26:27] op_sel_hi:[1,0,1]
	v_add_f32_e32 v105, v86, v87
	v_pk_add_f32 v[90:91], v[94:95], v[90:91]
	v_mov_b32_e32 v96, v80
	v_mov_b32_e32 v92, v81
	v_mov_b32_e32 v102, v88
	v_mov_b32_e32 v104, v89
	v_add_f32_e32 v94, v90, v91
	v_pk_add_f32 v[90:91], v[96:97], v[92:93]
	v_pk_add_f32 v[92:93], v[102:103], v[104:105]
	global_load_dwordx4 v[26:29], v[196:197], off
	global_load_dwordx4 v[54:57], v[198:199], off
	global_load_dwordx4 v[30:33], v[196:197], off offset:1024
	global_load_dwordx4 v[50:53], v[198:199], off offset:1024
	global_load_dwordx4 v[34:37], v[196:197], off offset:2048
	global_load_dwordx4 v[46:49], v[198:199], off offset:2048
	global_load_dwordx4 v[38:41], v[196:197], off offset:3072
	global_load_dwordx4 v[42:45], v[198:199], off offset:3072
	v_pk_add_f32 v[90:91], v[92:93], v[90:91]
	s_nop 0
	v_add_f32_e32 v90, v90, v91
	s_nop 1
	v_mov_b32_dpp v91, v94 quad_perm:[1,0,3,2] row_mask:0xf bank_mask:0xf
	s_nop 1
	v_mov_b32_dpp v92, v90 quad_perm:[1,0,3,2] row_mask:0xf bank_mask:0xf
	s_waitcnt lgkmcnt(1)
	v_add_f32_e32 v91, v94, v91
	s_waitcnt lgkmcnt(0)
	v_add_f32_e32 v90, v90, v92
	s_nop 1
	v_mov_b32_dpp v92, v91 quad_perm:[2,3,0,1] row_mask:0xf bank_mask:0xf
	s_nop 1
	v_mov_b32_dpp v93, v90 quad_perm:[2,3,0,1] row_mask:0xf bank_mask:0xf
	s_waitcnt lgkmcnt(1)
	v_add_f32_e32 v91, v91, v92
	s_nop 1
	v_mov_b32_dpp v92, v91 row_half_mirror row_mask:0xf bank_mask:0xf
	s_waitcnt lgkmcnt(1)
	v_add_f32_e32 v90, v90, v93
	s_nop 1
	v_mov_b32_dpp v93, v90 row_half_mirror row_mask:0xf bank_mask:0xf
	s_waitcnt lgkmcnt(1)
	v_add_f32_e32 v91, v91, v92
	s_nop 1
	v_mov_b32_dpp v92, v91 row_mirror row_mask:0xf bank_mask:0xf
	s_waitcnt lgkmcnt(1)
	v_add_f32_e32 v90, v90, v93
	s_nop 1
	v_mov_b32_dpp v93, v90 row_mirror row_mask:0xf bank_mask:0xf
	s_waitcnt lgkmcnt(1)
	v_add_f32_e32 v91, v91, v92
	v_mov_b32_e32 v92, v91
	s_nop 1
	v_permlane16_swap_b32_e32 v92, v91
	s_waitcnt lgkmcnt(1)
	v_add_f32_e32 v90, v90, v93
	v_mov_b32_e32 v93, v90
	s_nop 1
	v_permlane16_swap_b32_e32 v93, v90
	s_waitcnt lgkmcnt(1)
	v_add_f32_e32 v91, v91, v92
	v_mov_b32_e32 v92, v91
	s_nop 1
	v_permlane32_swap_b32_e32 v92, v91
	s_waitcnt lgkmcnt(1)
	v_add_f32_e32 v90, v90, v93
	v_mov_b32_e32 v93, v90
	s_nop 1
	v_permlane32_swap_b32_e32 v93, v90
	s_waitcnt lgkmcnt(1)
	v_add_f32_e32 v106, v91, v92
	v_fmamk_f32 v61, v106, 0xba800000, v61
	v_fmac_f32_e32 v60, 0xba800000, v106
	v_fmamk_f32 v63, v106, 0xba800000, v63
	v_fmac_f32_e32 v62, 0xba800000, v106
	s_waitcnt lgkmcnt(0)
	v_add_f32_e32 v107, v90, v93
	v_pk_mul_f32 v[90:91], v[62:63], v[62:63]
	v_pk_mul_f32 v[92:93], v[60:61], v[60:61]
	v_fmamk_f32 v59, v107, 0xba800000, v59
	v_fmac_f32_e32 v58, 0xba800000, v107
	v_fmamk_f32 v71, v107, 0xba800000, v71
	v_fmac_f32_e32 v70, 0xba800000, v107
	v_pk_mov_b32 v[94:95], v[92:93], v[90:91] op_sel:[1,0]
	v_mov_b32_e32 v93, v91
	v_pk_add_f32 v[90:91], v[94:95], v[92:93]
	v_pk_mul_f32 v[92:93], v[70:71], v[70:71]
	v_pk_mul_f32 v[94:95], v[58:59], v[58:59]
	v_fmamk_f32 v67, v106, 0xba800000, v67
	v_pk_mov_b32 v[96:97], v[94:95], v[92:93] op_sel:[1,0]
	v_mov_b32_e32 v95, v93
	v_fmac_f32_e32 v66, 0xba800000, v106
	v_fmamk_f32 v69, v106, 0xba800000, v69
	v_fmac_f32_e32 v68, 0xba800000, v106
	v_pk_add_f32 v[92:93], v[96:97], v[94:95]
	v_pk_mul_f32 v[94:95], v[68:69], v[68:69]
	v_pk_mul_f32 v[96:97], v[66:67], v[66:67]
	v_fmamk_f32 v65, v107, 0xba800000, v65
	v_fmac_f32_e32 v64, 0xba800000, v107
	v_fmamk_f32 v79, v107, 0xba800000, v79
	v_fmac_f32_e32 v78, 0xba800000, v107
	v_pk_mov_b32 v[98:99], v[96:97], v[94:95] op_sel:[1,0]
	v_mov_b32_e32 v97, v95
	v_pk_add_f32 v[90:91], v[90:91], v[90:91] op_sel_hi:[0,1]
	v_pk_add_f32 v[94:95], v[98:99], v[96:97]
	v_pk_mul_f32 v[96:97], v[78:79], v[78:79]
	v_pk_mul_f32 v[98:99], v[64:65], v[64:65]
	v_fmac_f32_e32 v74, 0xba800000, v106
	v_pk_mov_b32 v[100:101], v[98:99], v[96:97] op_sel:[1,0]
	v_mov_b32_e32 v99, v97
	v_fmamk_f32 v75, v106, 0xba800000, v75
	v_fmac_f32_e32 v76, 0xba800000, v106
	v_mul_f32_e32 v90, v74, v74
	v_pk_add_f32 v[96:97], v[100:101], v[98:99]
	v_fmamk_f32 v77, v106, 0xba800000, v77
	v_fmac_f32_e32 v72, 0xba800000, v107
	v_pk_fma_f32 v[98:99], v[74:75], v[74:75], v[90:91] op_sel_hi:[1,1,0]
	v_mul_f32_e32 v90, v76, v76
	v_fmamk_f32 v73, v107, 0xba800000, v73
	v_fmac_f32_e32 v86, 0xba800000, v107
	v_pk_fma_f32 v[100:101], v[76:77], v[76:77], v[90:91] op_sel_hi:[1,1,0]
	v_mul_f32_e32 v90, v72, v72
	v_pk_add_f32 v[94:95], v[94:95], v[94:95] op_sel_hi:[0,1]
	v_fmamk_f32 v87, v107, 0xba800000, v87
	v_pk_fma_f32 v[102:103], v[72:73], v[72:73], v[90:91] op_sel_hi:[1,1,0]
	v_mul_f32_e32 v90, v86, v86
	v_fmamk_f32 v85, v106, 0xba800000, v85
	v_fmac_f32_e32 v84, 0xba800000, v106
	v_fmamk_f32 v83, v106, 0xba800000, v83
	v_fmac_f32_e32 v82, 0xba800000, v106
	v_pk_fma_f32 v[104:105], v[86:87], v[86:87], v[90:91] op_sel_hi:[1,1,0]
	v_mul_f32_e32 v98, v82, v82
	v_mul_f32_e32 v100, v83, v83
	v_mul_f32_e32 v90, v84, v84
	v_mul_f32_e32 v94, v85, v85
	v_pk_add_f32 v[92:93], v[92:93], v[92:93] op_sel_hi:[0,1]
	v_pk_add_f32 v[96:97], v[96:97], v[96:97] op_sel_hi:[0,1]
	v_fmamk_f32 v89, v107, 0xba800000, v89
	v_fmac_f32_e32 v88, 0xba800000, v107
	v_fmamk_f32 v81, v107, 0xba800000, v81
	v_fmac_f32_e32 v80, 0xba800000, v107
	v_pk_add_f32 v[98:99], v[98:99], v[100:101]
	v_pk_add_f32 v[90:91], v[90:91], v[94:95]
	v_mul_f32_e32 v102, v80, v80
	v_pk_add_f32 v[90:91], v[98:99], v[90:91]
	v_mul_f32_e32 v104, v81, v81
	v_mul_f32_e32 v92, v88, v88
	v_mul_f32_e32 v96, v89, v89
	v_add_f32_e32 v94, v90, v91
	v_pk_add_f32 v[90:91], v[102:103], v[104:105]
	v_pk_add_f32 v[92:93], v[92:93], v[96:97]
	s_nop 0
	v_pk_add_f32 v[90:91], v[90:91], v[92:93]
	s_nop 0
	v_add_f32_e32 v90, v90, v91
	s_nop 1
	v_mov_b32_dpp v91, v94 quad_perm:[1,0,3,2] row_mask:0xf bank_mask:0xf
	s_nop 1
	v_mov_b32_dpp v92, v90 quad_perm:[1,0,3,2] row_mask:0xf bank_mask:0xf
	s_waitcnt lgkmcnt(1)
	v_add_f32_e32 v91, v94, v91
	s_waitcnt lgkmcnt(0)
	v_add_f32_e32 v90, v90, v92
	s_nop 1
	v_mov_b32_dpp v92, v91 quad_perm:[2,3,0,1] row_mask:0xf bank_mask:0xf
	s_nop 1
	v_mov_b32_dpp v93, v90 quad_perm:[2,3,0,1] row_mask:0xf bank_mask:0xf
	s_waitcnt lgkmcnt(1)
	v_add_f32_e32 v91, v91, v92
	s_waitcnt lgkmcnt(0)
	v_add_f32_e32 v90, v90, v93
	s_nop 1
	v_mov_b32_dpp v92, v91 row_half_mirror row_mask:0xf bank_mask:0xf
	s_nop 1
	v_mov_b32_dpp v93, v90 row_half_mirror row_mask:0xf bank_mask:0xf
	s_waitcnt lgkmcnt(1)
	v_add_f32_e32 v91, v91, v92
	s_waitcnt lgkmcnt(0)
	v_add_f32_e32 v90, v90, v93
	s_nop 1
	v_mov_b32_dpp v92, v91 row_mirror row_mask:0xf bank_mask:0xf
	s_nop 1
	v_mov_b32_dpp v93, v90 row_mirror row_mask:0xf bank_mask:0xf
	s_waitcnt lgkmcnt(1)
	v_add_f32_e32 v91, v91, v92
	s_waitcnt lgkmcnt(0)
	v_add_f32_e32 v90, v90, v93
	v_mov_b32_e32 v92, v91
	s_nop 1
	v_permlane16_swap_b32_e32 v92, v91
	v_mov_b32_e32 v93, v90
	s_nop 1
	v_permlane16_swap_b32_e32 v93, v90
	s_waitcnt lgkmcnt(1)
	v_add_f32_e32 v91, v91, v92
	s_waitcnt lgkmcnt(0)
	v_add_f32_e32 v90, v90, v93
	v_mov_b32_e32 v92, v91
	s_nop 1
	v_permlane32_swap_b32_e32 v92, v91
	v_mov_b32_e32 v93, v90
	s_nop 1
	v_permlane32_swap_b32_e32 v93, v90
	s_waitcnt lgkmcnt(1)
	v_add_f32_e32 v91, v91, v92
	s_waitcnt lgkmcnt(0)
	v_add_f32_e32 v90, v90, v93
	v_fmamk_f32 v91, v91, 0x3a800000, v226
	v_rsq_f32_e32 v94, v91
	v_fmamk_f32 v90, v90, 0x3a800000, v226
	v_rsq_f32_e32 v96, v90
	v_pk_mul_f32 v[60:61], v[60:61], v[94:95] op_sel_hi:[1,0]
	v_pk_mul_f32 v[62:63], v[62:63], v[94:95] op_sel_hi:[1,0]
	s_waitcnt vmcnt(6)
	v_pk_fma_f32 v[90:91], v[26:27], v[60:61], v[54:55]
	v_pk_mul_f32 v[58:59], v[58:59], v[96:97] op_sel_hi:[1,0]
	v_pk_mul_f32 v[60:61], v[70:71], v[96:97] op_sel_hi:[1,0]
	v_pk_fma_f32 v[92:93], v[28:29], v[62:63], v[56:57]
	v_pk_fma_f32 v[28:29], v[28:29], v[60:61], v[56:57]
	v_pk_fma_f32 v[26:27], v[26:27], v[58:59], v[54:55]
	v_pk_mul_f32 v[54:55], v[66:67], v[94:95] op_sel_hi:[1,0]
	v_pk_mul_f32 v[56:57], v[68:69], v[94:95] op_sel_hi:[1,0]
	s_waitcnt vmcnt(4)
	v_pk_fma_f32 v[110:111], v[30:31], v[54:55], v[50:51]
	v_pk_fma_f32 v[112:113], v[32:33], v[56:57], v[52:53]
	v_pk_mul_f32 v[54:55], v[64:65], v[96:97] op_sel_hi:[1,0]
	v_pk_mul_f32 v[56:57], v[78:79], v[96:97] op_sel_hi:[1,0]
	v_pk_fma_f32 v[30:31], v[30:31], v[54:55], v[50:51]
	v_pk_fma_f32 v[32:33], v[32:33], v[56:57], v[52:53]
	v_pk_mul_f32 v[50:51], v[74:75], v[94:95] op_sel_hi:[1,0]
	v_pk_mul_f32 v[52:53], v[76:77], v[94:95] op_sel_hi:[1,0]
	s_waitcnt vmcnt(2)
	v_pk_fma_f32 v[130:131], v[34:35], v[50:51], v[46:47]
	v_pk_fma_f32 v[132:133], v[36:37], v[52:53], v[48:49]
	v_pk_mul_f32 v[50:51], v[72:73], v[96:97] op_sel_hi:[1,0]
	v_pk_mul_f32 v[52:53], v[86:87], v[96:97] op_sel_hi:[1,0]
	v_pk_fma_f32 v[34:35], v[34:35], v[50:51], v[46:47]
	v_pk_fma_f32 v[36:37], v[36:37], v[52:53], v[48:49]
	v_pk_mul_f32 v[46:47], v[82:83], v[94:95] op_sel_hi:[1,0]
	v_pk_mul_f32 v[48:49], v[84:85], v[94:95] op_sel_hi:[1,0]
	s_waitcnt vmcnt(0)
	v_pk_fma_f32 v[142:143], v[38:39], v[46:47], v[42:43]
	v_pk_fma_f32 v[144:145], v[40:41], v[48:49], v[44:45]
	v_pk_mul_f32 v[46:47], v[80:81], v[96:97] op_sel_hi:[1,0]
	v_pk_mul_f32 v[48:49], v[88:89], v[96:97] op_sel_hi:[1,0]
	v_pk_fma_f32 v[38:39], v[38:39], v[46:47], v[42:43]
	v_pk_fma_f32 v[40:41], v[40:41], v[48:49], v[44:45]
	s_cbranch_vccnz .LBB0_1574
	s_add_i32 s24, s50, 1
	s_ashr_i32 s51, s50, 31
	s_ashr_i32 s25, s24, 31
	s_lshl_b64 s[14:15], s[50:51], 12
	s_lshl_b64 s[24:25], s[24:25], 12
	v_lshl_add_u64 v[42:43], v[208:209], 0, s[14:15]
	v_lshl_add_u64 v[44:45], v[208:209], 0, s[24:25]
	global_store_dwordx4 v[42:43], v[90:93], off
	global_store_dwordx4 v[44:45], v[26:29], off
	global_store_dwordx4 v[42:43], v[110:113], off offset:1024
	global_store_dwordx4 v[44:45], v[30:33], off offset:1024
	global_store_dwordx4 v[42:43], v[130:133], off offset:2048
	global_store_dwordx4 v[44:45], v[34:37], off offset:2048
	global_store_dwordx4 v[42:43], v[142:145], off offset:3072
	global_store_dwordx4 v[44:45], v[38:41], off offset:3072
